# GEMM2 walks the experts in reverse (the most recently written HID panels first, still cache resident)
# speedup vs baseline: 1.0169x; 1.0169x over previous
;     __device__ bool next(int i, Unit& u) const {
;         const long L = (long)i * G + c; if (L >= total) return false;
;         if (mode == 1) { const int x = c & 7, j = c >> 3; u.g = 4 * i + (x >> 1); u.pm = 8 * (x & 1) + (j >> 2); u.pn = j & 3; return true; }
.LBB0_1082:
	s_lshl_b32 s2, s92, 3
	s_and_b32 s2, s2, 8
	s_ashr_i32 s3, s92, 5
	s_bfe_u32 s18, s92, 0x20001
	s_or_b32 s18, s18, 12
	s_add_i32 s48, s2, s3
	s_bfe_u32 s19, s92, 0x20003

;     __device__ bool next(int i, Unit& u) const {
;         const long L = (long)i * G + c; if (L >= total) return false;
;         if (mode == 1) { const int x = c & 7, j = c >> 3; u.g = 4 * i + (x >> 1); u.pm = 8 * (x & 1) + (j >> 2); u.pn = j & 3; return true; }
; template <bool BF, bool GATHER = false, class Epi, class Hook>
; __device__ __forceinline__ void gemm_phase(LAS unsigned char* lds, const Gemm g, const Order& S, const Epi& E, Hook& HK) {
;     ...
;         const bool has_next = S.next(ui + 1, nxt);
;         const char* nA = GATHER ? cA : (has_next ? (const char*)(g.A + (size_t)nxt.g * g.sA) + (size_t)nxt.pm * tstep : cA); const char* nB = has_next ? (const char*)(g.Bt + (size_t)nxt.g * g.sB) + (size_t)nxt.pn * tstep : cB;
.LBB0_1095:
	s_and_b64 vcc, exec, s[20:21]
	s_cbranch_vccz .LBB0_1097
	s_sub_i32 s4, 3, s34
	s_lshl_b32 s4, s4, 2
	s_or_b32 s16, s4, s39
	s_mov_b32 s17, s40
	s_mov_b32 s47, s41

;     __device__ bool next(int i, Unit& u) const {
;         const long L = (long)i * G + c; if (L >= total) return false;
;         if (mode == 1) { const int x = c & 7, j = c >> 3; u.g = 4 * i + (x >> 1); u.pm = 8 * (x & 1) + (j >> 2); u.pn = j & 3; return true; }
.LBB0_1847:
	s_lshl_b32 s2, s92, 3
	s_and_b32 s2, s2, 8
	s_ashr_i32 s3, s92, 5
	s_bfe_u32 s16, s92, 0x20001
	s_or_b32 s16, s16, 12
	s_add_i32 s49, s2, s3
	s_bfe_u32 s17, s92, 0x20003

;     __device__ bool next(int i, Unit& u) const {
;         const long L = (long)i * G + c; if (L >= total) return false;
;         if (mode == 1) { const int x = c & 7, j = c >> 3; u.g = 4 * i + (x >> 1); u.pm = 8 * (x & 1) + (j >> 2); u.pn = j & 3; return true; }
; template <bool BF, bool GATHER = false, class Epi, class Hook>
; __device__ __forceinline__ void gemm_phase(LAS unsigned char* lds, const Gemm g, const Order& S, const Epi& E, Hook& HK) {
;     ...
;         const bool has_next = S.next(ui + 1, nxt);
;         const char* nA = GATHER ? cA : (has_next ? (const char*)(g.A + (size_t)nxt.g * g.sA) + (size_t)nxt.pm * tstep : cA); const char* nB = has_next ? (const char*)(g.Bt + (size_t)nxt.g * g.sB) + (size_t)nxt.pn * tstep : cB;
.LBB0_1860:
	s_and_b64 vcc, exec, s[20:21]
	s_cbranch_vccz .LBB0_1862
	s_sub_i32 s4, 3, s34
	s_lshl_b32 s4, s4, 2
	s_or_b32 s18, s4, s40
	s_mov_b32 s19, s41
	s_mov_b32 s48, s42
